# attention pool work counters moved to separate 4 KiB-strided cache lines in the zeroed control area (was 8 counters in one line) to stop same-line atomic serialisation
# speedup vs baseline: 1.0423x; 1.0369x over previous
.LBB0_523:
	s_waitcnt lgkmcnt(0)
	s_cmp_le_i32 s94, s4
	s_cselect_b64 s[0:1], -1, 0
	s_cmp_lt_i32 s4, s95
	s_cselect_b64 s[6:7], -1, 0
	s_and_b64 s[0:1], s[0:1], s[6:7]
	s_andn2_b64 vcc, exec, s[0:1]
	s_mov_b64 s[0:1], 0
	v_writelane_b32 v254, s0, 42
	s_mov_b64 s[42:43], 0
	s_nop 0
	v_writelane_b32 v254, s1, 43
	s_cbranch_vccnz .LBB0_602
	s_mov_b64 s[0:1], s[90:91]
	v_mbcnt_lo_u32_b32 v142, -1, 0
	v_mbcnt_hi_u32_b32 v142, -1, v142
	v_readlane_b32 s8, v253, 0
	s_load_dwordx2 s[0:1], s[0:1], 0xb8
	s_waitcnt lgkmcnt(0)
	s_add_u32 s44, s0, 0x24a00000
	s_addc_u32 s45, s1, 0
	s_add_u32 s46, s0, 0x23600000
	s_addc_u32 s47, s1, 0
	s_add_u32 s48, s0, 0x39a00000
	s_addc_u32 s49, s1, 0
	s_add_u32 s50, s0, 0x3a200000
	v_readlane_b32 s4, v254, 37
	s_addc_u32 s51, s1, 0
	s_lshl_b32 s4, s4, 6
	s_lshl_b64 s[6:7], s[4:5], 2
	s_add_u32 s4, s0, s6
	s_addc_u32 s6, s1, s7
	s_add_u32 s4, s4, 0x20000
	s_mulk_i32 s8, 0x4c00
	s_addc_u32 s12, s6, 0
	s_add_i32 s6, s8, 0
	s_waitcnt vmcnt(0)
	v_lshlrev_b32_e32 v1, 4, v142
	v_and_b32_e32 v2, 15, v142
	v_ashrrev_i32_e32 v0, 4, v142
	v_and_b32_e32 v161, 0x70, v1
	v_mov_b32_e32 v1, s6
	v_mad_u32_u24 v3, v2, s3, v1
	v_lshlrev_b32_e32 v5, 2, v0
	v_bfe_u32 v1, v142, 2, 2
	v_or_b32_e32 v6, v5, v1
	v_mul_lo_u32 v1, v6, s3
	v_add_u32_e32 v7, s6, v1
	v_lshlrev_b32_e32 v1, 3, v142
	v_and_b32_e32 v8, 24, v1
	v_lshlrev_b32_e32 v1, 8, v0
	v_lshlrev_b32_e32 v136, 4, v2
	v_lshlrev_b32_e32 v4, 3, v0
	v_add3_u32 v168, s6, v1, v136
	v_lshlrev_b32_e32 v169, 7, v0
	v_lshl_add_u64 v[0:1], s[0:1], 0, v[136:137]
	s_mov_b64 s[0:1], 0x31a00000
	v_ashrrev_i32_e32 v160, 3, v142
	v_lshl_add_u64 v[146:147], v[0:1], 0, s[0:1]
	v_mul_lo_u32 v1, v6, s62
	v_and_b32_e32 v164, -16, v142
	v_add3_u32 v174, s6, v1, v8
	v_mul_u32_u24_e32 v1, 0x120, v2
	v_mul_lo_u32 v176, v160, s3
	v_ashrrev_i32_e32 v143, 31, v142
	v_lshl_add_u32 v165, v160, 1, s6
	v_add_u32_e32 v167, s6, v161
	v_lshlrev_b32_e32 v0, 2, v142
	v_add3_u32 v175, s6, v1, v164
	v_lshlrev_b32_e32 v1, 1, v176
	s_add_i32 s13, s6, 0x4800
	s_getreg_b32 s14, hwreg(HW_REG_XCC_ID, 0, 4)
	s_mov_b32 s15, 0
	v_cmp_eq_u32_e64 s[36:37], 0, v142
	s_add_i32 s28, s6, 0x4a00
	v_lshl_add_u64 v[144:145], v[142:143], 1, s[46:47]
	v_lshl_add_u32 v162, v142, 1, s6
	v_cmp_gt_u32_e64 s[38:39], 4, v2
	v_lshlrev_b32_e32 v163, 7, v2
	v_add_u32_e32 v166, 0x4800, v165
	v_cmp_gt_u32_e64 s[40:41], 16, v142
	v_add_u32_e32 v170, 64, v142
	v_add_u32_e32 v171, 0x80, v142
	v_add_u32_e32 v172, 0xc0, v142
	v_lshl_add_u32 v173, v2, 8, v164
	v_add3_u32 v177, v167, v161, v1
	v_add_u32_e32 v178, 19, v5
	v_add_u32_e32 v179, v3, v4
	v_add_u32_e32 v180, s6, v0
	v_add_u32_e32 v181, v7, v8
	s_branch .LBB0_526

.LBB0_526:
	s_add_i32 s10, s15, s14
	s_and_b32 s11, s10, 7
	s_lshl_b32 s0, s11, 12
	s_add_u32 s52, s4, s0
	s_addc_u32 s53, s12, 0
	s_waitcnt vmcnt(16)
	v_mov_b32_e32 v0, 0
	s_and_saveexec_b64 s[0:1], s[36:37]
	s_cbranch_execz .LBB0_530
	s_mov_b64 s[8:9], exec
	v_mbcnt_lo_u32_b32 v0, s8, 0
	v_mbcnt_hi_u32_b32 v0, s9, v0
	v_cmp_eq_u32_e32 vcc, 0, v0
	s_and_saveexec_b64 s[6:7], vcc
	s_cbranch_execz .LBB0_529
	s_bcnt1_i32_b64 s8, s[8:9]
	s_lshl_b32 s8, s8, 2
	v_mov_b32_e32 v1, s8
	global_atomic_add v1, v137, v1, s[52:53] sc0
